# speedup vs baseline: 1.5224x; 1.0066x over previous
_Z6prep_k5PrepP:
	s_cmp_lt_u32 s2, 0x100
	s_cbranch_scc1 .Lprep_conv1
	s_sub_u32 s20, s2, 0x100
	s_lshl_b32 s20, s20, 8
	s_mov_b32 s21, 0
.Lprep_e:
	s_cmp_lt_u32 s20, 73728
	s_cbranch_scc0 .Lprep_seg1
	s_load_dwordx2 s[24:25], s[0:1], 24
	s_load_dwordx2 s[26:27], s[0:1], 88
	s_mov_b32 s22, s20
	s_mov_b32 s23, 1
	s_mov_b32 s28, 6
	s_mov_b32 s29, 7
	s_mov_b32 s30, 63
	s_branch .Lprep_go
.Lprep_seg1:
	s_cmp_lt_u32 s20, 368640
	s_cbranch_scc0 .Lprep_seg2
	s_load_dwordx2 s[24:25], s[0:1], 32
	s_load_dwordx2 s[26:27], s[0:1], 96
	s_sub_u32 s22, s20, 73728
	s_mov_b32 s23, 1
	s_mov_b32 s28, 7
	s_mov_b32 s29, 8
	s_mov_b32 s30, 127
	s_branch .Lprep_go
.Lprep_seg2:
	s_cmp_lt_u32 s20, 630784
	s_cbranch_scc0 .Lprep_seg3
	s_load_dwordx2 s[24:25], s[0:1], 40
	s_load_dwordx2 s[26:27], s[0:1], 104
	s_sub_u32 s22, s20, 368640
	s_mov_b32 s23, 0
	s_branch .Lprep_go
.Lprep_seg3:
	s_cmp_lt_u32 s20, 729088
	s_cbranch_scc0 .Lprep_seg4
	s_load_dwordx2 s[24:25], s[0:1], 48
	s_load_dwordx2 s[26:27], s[0:1], 112
	s_sub_u32 s22, s20, 630784
	s_mov_b32 s23, 3
	s_branch .Lprep_go
.Lprep_seg4:
	s_cmp_lt_u32 s20, 860160
	s_cbranch_scc0 .Lprep_seg5
	s_load_dwordx2 s[24:25], s[0:1], 56
	s_load_dwordx2 s[26:27], s[0:1], 120
	s_sub_u32 s22, s20, 729088
	s_mov_b32 s23, 0
	s_branch .Lprep_go
.Lprep_seg5:
	s_cmp_lt_u32 s20, 1155072
	s_cbranch_scc0 .Lprep_seg6
	s_load_dwordx2 s[24:25], s[0:1], 64
	s_load_dwordx2 s[26:27], s[0:1], 128
	s_sub_u32 s22, s20, 860160
	s_mov_b32 s23, 2
	s_mov_b32 s28, 8
	s_mov_b32 s29, 7
	s_mov_b32 s30, 255
	s_branch .Lprep_go
.Lprep_seg6:
	s_load_dwordx2 s[24:25], s[0:1], 72
	s_load_dwordx2 s[26:27], s[0:1], 136
	s_sub_u32 s22, s20, 1155072
	s_mov_b32 s23, 2
	s_mov_b32 s28, 7
	s_mov_b32 s29, 6
	s_mov_b32 s30, 127
.Lprep_go:
	v_add_u32_e32 v1, s22, v0
	v_lshlrev_b32_e32 v2, 1, v1
	v_mov_b32_e32 v4, 0
	s_cmp_eq_u32 s23, 0
	s_cbranch_scc1 .Lprep_plain
	s_cmp_eq_u32 s23, 3
	s_cbranch_scc1 .Lprep_xp
	v_lshrrev_b32_e32 v5, s28, v1
	v_mul_u32_u24_e32 v6, 0x1c72, v5
	v_lshrrev_b32_e32 v6, 16, v6
	v_mul_u32_u24_e32 v7, 9, v6
	v_sub_u32_e32 v7, v5, v7
	v_and_b32_e32 v8, s30, v1
	s_cmp_eq_u32 s23, 1
	s_cbranch_scc0 .Lprep_dec
	v_lshl_add_u32 v9, v6, s28, v8
	v_mul_u32_u24_e32 v9, 9, v9
	v_add_u32_e32 v3, v9, v7
	s_branch .Lprep_ld
.Lprep_dec:
	v_lshl_add_u32 v9, v8, s29, v6
	v_mul_u32_u24_e32 v9, 9, v9
	v_sub_u32_e32 v7, 8, v7
	v_add_u32_e32 v3, v9, v7
	s_branch .Lprep_ld
.Lprep_xp:
	s_cmp_lt_u32 s22, 73728
	s_cbranch_scc0 .Lprep_st
.Lprep_plain:
	v_mov_b32_e32 v3, v1
.Lprep_ld:
	v_lshlrev_b32_e32 v3, 2, v3
	s_waitcnt lgkmcnt(0)
	global_load_dword v4, v3, s[24:25]
	s_waitcnt vmcnt(0)
	v_cvt_f16_f32_e32 v4, v4
.Lprep_st:
	s_waitcnt lgkmcnt(0)
	global_store_short v2, v4, s[26:27]
	s_add_u32 s20, s20, 307200
	s_add_u32 s21, s21, 1
	s_cmp_lt_u32 s21, 4
	s_cbranch_scc1 .Lprep_e
	s_endpgm
.Lprep_conv1:
	s_load_dwordx4 s[8:11], s[0:1], 0x0
	s_load_dwordx2 s[12:13], s[0:1], 0x10
	s_load_dwordx2 s[14:15], s[0:1], 0x50
	s_load_dwordx2 s[16:17], s[0:1], 0x90
	v_lshlrev_b32_e32 v1, 2, v0
	v_add_u32_e32 v2, 0x1000, v1
	s_waitcnt lgkmcnt(0)
	global_load_dword v28, v1, s[10:11]
	global_load_dword v29, v1, s[10:11] offset:1024
	global_load_dword v30, v1, s[10:11] offset:2048
	global_load_dword v31, v1, s[10:11] offset:3072
	global_load_dword v32, v2, s[10:11]
	global_load_dword v33, v2, s[10:11] offset:1024
	v_cmp_gt_u32_e32 vcc, 0xc0, v0
	s_and_saveexec_b64 s[18:19], vcc
	global_load_dword v34, v2, s[10:11] offset:2048
	s_mov_b64 exec, s[18:19]
	v_cmp_gt_u32_e32 vcc, 64, v0
	s_and_saveexec_b64 s[20:21], vcc
	global_load_dword v35, v1, s[12:13]
	s_mov_b64 exec, s[20:21]
	s_cmp_lg_u32 s2, 0
	s_cbranch_scc1 .Lprep_nz
	v_mov_b32_e32 v3, 0
	global_store_dword v1, v3, s[16:17]
.Lprep_nz:
	v_and_b32_e32 v4, 7, v0
	v_lshrrev_b32_e32 v5, 3, v0
	s_lshl_b32 s22, s2, 5
	v_add_u32_e32 v5, s22, v5
	v_and_b32_e32 v6, 63, v5
	v_bfe_u32 v7, v5, 6, 6
	v_lshrrev_b32_e32 v8, 12, v5
	v_mul_u32_u24_e32 v8, 0x3000, v8
	v_lshl_add_u32 v3, v7, 6, v6
	v_add_u32_e32 v56, -1, v7
	v_add_u32_e32 v57, -1, v6
	v_max_u32_e32 v58, v56, v57
	v_cmp_gt_u32_e64 s[40:41], 64, v58
	v_lshl_add_u32 v59, v56, 6, v57
	s_nop 1
	v_cndmask_b32_e64 v59, v3, v59, s[40:41]
	v_add_u32_e32 v59, v8, v59
	v_lshlrev_b32_e32 v10, 2, v59
	v_add_u32_e32 v56, -1, v7
	v_add_u32_e32 v57, 0, v6
	v_max_u32_e32 v58, v56, v57
	v_cmp_gt_u32_e64 s[42:43], 64, v58
	v_lshl_add_u32 v59, v56, 6, v57
	s_nop 1
	v_cndmask_b32_e64 v59, v3, v59, s[42:43]
	v_add_u32_e32 v59, v8, v59
	v_lshlrev_b32_e32 v11, 2, v59
	v_add_u32_e32 v56, -1, v7
	v_add_u32_e32 v57, 1, v6
	v_max_u32_e32 v58, v56, v57
	v_cmp_gt_u32_e64 s[44:45], 64, v58
	v_lshl_add_u32 v59, v56, 6, v57
	s_nop 1
	v_cndmask_b32_e64 v59, v3, v59, s[44:45]
	v_add_u32_e32 v59, v8, v59
	v_lshlrev_b32_e32 v12, 2, v59
	v_add_u32_e32 v56, 0, v7
	v_add_u32_e32 v57, -1, v6
	v_max_u32_e32 v58, v56, v57
	v_cmp_gt_u32_e64 s[46:47], 64, v58
	v_lshl_add_u32 v59, v56, 6, v57
	s_nop 1
	v_cndmask_b32_e64 v59, v3, v59, s[46:47]
	v_add_u32_e32 v59, v8, v59
	v_lshlrev_b32_e32 v13, 2, v59
	v_add_u32_e32 v56, 0, v7
	v_add_u32_e32 v57, 0, v6
	v_max_u32_e32 v58, v56, v57
	v_cmp_gt_u32_e64 s[48:49], 64, v58
	v_lshl_add_u32 v59, v56, 6, v57
	s_nop 1
	v_cndmask_b32_e64 v59, v3, v59, s[48:49]
	v_add_u32_e32 v59, v8, v59
	v_lshlrev_b32_e32 v14, 2, v59
	v_add_u32_e32 v56, 0, v7
	v_add_u32_e32 v57, 1, v6
	v_max_u32_e32 v58, v56, v57
	v_cmp_gt_u32_e64 s[50:51], 64, v58
	v_lshl_add_u32 v59, v56, 6, v57
	s_nop 1
	v_cndmask_b32_e64 v59, v3, v59, s[50:51]
	v_add_u32_e32 v59, v8, v59
	v_lshlrev_b32_e32 v15, 2, v59
	v_add_u32_e32 v56, 1, v7
	v_add_u32_e32 v57, -1, v6
	v_max_u32_e32 v58, v56, v57
	v_cmp_gt_u32_e64 s[52:53], 64, v58
	v_lshl_add_u32 v59, v56, 6, v57
	s_nop 1
	v_cndmask_b32_e64 v59, v3, v59, s[52:53]
	v_add_u32_e32 v59, v8, v59
	v_lshlrev_b32_e32 v16, 2, v59
	v_add_u32_e32 v56, 1, v7
	v_add_u32_e32 v57, 0, v6
	v_max_u32_e32 v58, v56, v57
	v_cmp_gt_u32_e64 s[54:55], 64, v58
	v_lshl_add_u32 v59, v56, 6, v57
	s_nop 1
	v_cndmask_b32_e64 v59, v3, v59, s[54:55]
	v_add_u32_e32 v59, v8, v59
	v_lshlrev_b32_e32 v17, 2, v59
	v_add_u32_e32 v56, 1, v7
	v_add_u32_e32 v57, 1, v6
	v_max_u32_e32 v58, v56, v57
	v_cmp_gt_u32_e64 s[56:57], 64, v58
	v_lshl_add_u32 v59, v56, 6, v57
	s_nop 1
	v_cndmask_b32_e64 v59, v3, v59, s[56:57]
	v_add_u32_e32 v59, v8, v59
	v_lshlrev_b32_e32 v18, 2, v59
	global_load_dword v19, v10, s[8:9]
	global_load_dword v20, v11, s[8:9]
	global_load_dword v21, v12, s[8:9]
	global_load_dword v22, v13, s[8:9]
	global_load_dword v23, v14, s[8:9]
	global_load_dword v24, v15, s[8:9]
	global_load_dword v25, v16, s[8:9]
	global_load_dword v26, v17, s[8:9]
	global_load_dword v27, v18, s[8:9]
	v_add_u32_e32 v56, 0, v0
	v_mul_u32_u24_e32 v57, 0x97c, v56
	v_lshrrev_b32_e32 v57, 16, v57
	v_mul_u32_u24_e32 v58, 27, v57
	v_sub_u32_e32 v58, v56, v58
	v_lshl_add_u32 v58, v58, 6, v57
	v_lshlrev_b32_e32 v48, 2, v58
	v_add_u32_e32 v56, 256, v0
	v_mul_u32_u24_e32 v57, 0x97c, v56
	v_lshrrev_b32_e32 v57, 16, v57
	v_mul_u32_u24_e32 v58, 27, v57
	v_sub_u32_e32 v58, v56, v58
	v_lshl_add_u32 v58, v58, 6, v57
	v_lshlrev_b32_e32 v49, 2, v58
	v_add_u32_e32 v56, 512, v0
	v_mul_u32_u24_e32 v57, 0x97c, v56
	v_lshrrev_b32_e32 v57, 16, v57
	v_mul_u32_u24_e32 v58, 27, v57
	v_sub_u32_e32 v58, v56, v58
	v_lshl_add_u32 v58, v58, 6, v57
	v_lshlrev_b32_e32 v50, 2, v58
	v_add_u32_e32 v56, 768, v0
	v_mul_u32_u24_e32 v57, 0x97c, v56
	v_lshrrev_b32_e32 v57, 16, v57
	v_mul_u32_u24_e32 v58, 27, v57
	v_sub_u32_e32 v58, v56, v58
	v_lshl_add_u32 v58, v58, 6, v57
	v_lshlrev_b32_e32 v51, 2, v58
	v_add_u32_e32 v56, 1024, v0
	v_mul_u32_u24_e32 v57, 0x97c, v56
	v_lshrrev_b32_e32 v57, 16, v57
	v_mul_u32_u24_e32 v58, 27, v57
	v_sub_u32_e32 v58, v56, v58
	v_lshl_add_u32 v58, v58, 6, v57
	v_lshlrev_b32_e32 v52, 2, v58
	v_add_u32_e32 v56, 1280, v0
	v_mul_u32_u24_e32 v57, 0x97c, v56
	v_lshrrev_b32_e32 v57, 16, v57
	v_mul_u32_u24_e32 v58, 27, v57
	v_sub_u32_e32 v58, v56, v58
	v_lshl_add_u32 v58, v58, 6, v57
	v_lshlrev_b32_e32 v53, 2, v58
	v_add_u32_e32 v56, 1536, v0
	v_mul_u32_u24_e32 v57, 0x97c, v56
	v_lshrrev_b32_e32 v57, 16, v57
	v_mul_u32_u24_e32 v58, 27, v57
	v_sub_u32_e32 v58, v56, v58
	v_lshl_add_u32 v58, v58, 6, v57
	v_lshlrev_b32_e32 v54, 2, v58
	s_waitcnt vmcnt(9)
	ds_write_b32 v48, v28
	ds_write_b32 v49, v29
	ds_write_b32 v50, v30
	ds_write_b32 v51, v31
	ds_write_b32 v52, v32
	ds_write_b32 v53, v33
	v_cmp_gt_u32_e32 vcc, 0xc0, v0
	s_and_saveexec_b64 s[18:19], vcc
	ds_write_b32 v54, v34
	s_mov_b64 exec, s[18:19]
	v_cmp_gt_u32_e32 vcc, 64, v0
	s_and_saveexec_b64 s[20:21], vcc
	ds_write_b32 v1, v35 offset:6912
	s_mov_b64 exec, s[20:21]
	s_waitcnt lgkmcnt(0)
	s_barrier
	v_lshlrev_b32_e32 v9, 5, v4
	ds_read_b128 v[40:43], v9 offset:6912
	ds_read_b128 v[44:47], v9 offset:6928
	s_mov_b32 s23, 0
	s_mov_b32 s24, 0x4000
.Lprep_ci:
	s_cmp_lt_u32 s23, 2
	s_cselect_b32 s25, s24, 0
	v_add_u32_e32 v10, s25, v10
	v_add_u32_e32 v11, s25, v11
	v_add_u32_e32 v12, s25, v12
	v_add_u32_e32 v13, s25, v13
	v_add_u32_e32 v14, s25, v14
	v_add_u32_e32 v15, s25, v15
	v_add_u32_e32 v16, s25, v16
	v_add_u32_e32 v17, s25, v17
	v_add_u32_e32 v18, s25, v18
	s_waitcnt vmcnt(0)
	v_cndmask_b32_e64 v28, 0, v19, s[40:41]
	v_cndmask_b32_e64 v29, 0, v20, s[42:43]
	v_cndmask_b32_e64 v30, 0, v21, s[44:45]
	v_cndmask_b32_e64 v31, 0, v22, s[46:47]
	v_cndmask_b32_e64 v32, 0, v23, s[48:49]
	v_cndmask_b32_e64 v33, 0, v24, s[50:51]
	v_cndmask_b32_e64 v34, 0, v25, s[52:53]
	v_cndmask_b32_e64 v35, 0, v26, s[54:55]
	v_cndmask_b32_e64 v36, 0, v27, s[56:57]
	global_load_dword v19, v10, s[8:9]
	global_load_dword v20, v11, s[8:9]
	global_load_dword v21, v12, s[8:9]
	global_load_dword v22, v13, s[8:9]
	global_load_dword v23, v14, s[8:9]
	global_load_dword v24, v15, s[8:9]
	global_load_dword v25, v16, s[8:9]
	global_load_dword v26, v17, s[8:9]
	global_load_dword v27, v18, s[8:9]
	ds_read_b128 v[48:51], v9 offset:0
	ds_read_b128 v[52:55], v9 offset:16
	s_waitcnt lgkmcnt(0)
	v_fmac_f32_e32 v40, v28, v48
	v_fmac_f32_e32 v41, v28, v49
	v_fmac_f32_e32 v42, v28, v50
	v_fmac_f32_e32 v43, v28, v51
	v_fmac_f32_e32 v44, v28, v52
	v_fmac_f32_e32 v45, v28, v53
	v_fmac_f32_e32 v46, v28, v54
	v_fmac_f32_e32 v47, v28, v55
	ds_read_b128 v[48:51], v9 offset:256
	ds_read_b128 v[52:55], v9 offset:272
	s_waitcnt lgkmcnt(0)
	v_fmac_f32_e32 v40, v29, v48
	v_fmac_f32_e32 v41, v29, v49
	v_fmac_f32_e32 v42, v29, v50
	v_fmac_f32_e32 v43, v29, v51
	v_fmac_f32_e32 v44, v29, v52
	v_fmac_f32_e32 v45, v29, v53
	v_fmac_f32_e32 v46, v29, v54
	v_fmac_f32_e32 v47, v29, v55
	ds_read_b128 v[48:51], v9 offset:512
	ds_read_b128 v[52:55], v9 offset:528
	s_waitcnt lgkmcnt(0)
	v_fmac_f32_e32 v40, v30, v48
	v_fmac_f32_e32 v41, v30, v49
	v_fmac_f32_e32 v42, v30, v50
	v_fmac_f32_e32 v43, v30, v51
	v_fmac_f32_e32 v44, v30, v52
	v_fmac_f32_e32 v45, v30, v53
	v_fmac_f32_e32 v46, v30, v54
	v_fmac_f32_e32 v47, v30, v55
	ds_read_b128 v[48:51], v9 offset:768
	ds_read_b128 v[52:55], v9 offset:784
	s_waitcnt lgkmcnt(0)
	v_fmac_f32_e32 v40, v31, v48
	v_fmac_f32_e32 v41, v31, v49
	v_fmac_f32_e32 v42, v31, v50
	v_fmac_f32_e32 v43, v31, v51
	v_fmac_f32_e32 v44, v31, v52
	v_fmac_f32_e32 v45, v31, v53
	v_fmac_f32_e32 v46, v31, v54
	v_fmac_f32_e32 v47, v31, v55
	ds_read_b128 v[48:51], v9 offset:1024
	ds_read_b128 v[52:55], v9 offset:1040
	s_waitcnt lgkmcnt(0)
	v_fmac_f32_e32 v40, v32, v48
	v_fmac_f32_e32 v41, v32, v49
	v_fmac_f32_e32 v42, v32, v50
	v_fmac_f32_e32 v43, v32, v51
	v_fmac_f32_e32 v44, v32, v52
	v_fmac_f32_e32 v45, v32, v53
	v_fmac_f32_e32 v46, v32, v54
	v_fmac_f32_e32 v47, v32, v55
	ds_read_b128 v[48:51], v9 offset:1280
	ds_read_b128 v[52:55], v9 offset:1296
	s_waitcnt lgkmcnt(0)
	v_fmac_f32_e32 v40, v33, v48
	v_fmac_f32_e32 v41, v33, v49
	v_fmac_f32_e32 v42, v33, v50
	v_fmac_f32_e32 v43, v33, v51
	v_fmac_f32_e32 v44, v33, v52
	v_fmac_f32_e32 v45, v33, v53
	v_fmac_f32_e32 v46, v33, v54
	v_fmac_f32_e32 v47, v33, v55
	ds_read_b128 v[48:51], v9 offset:1536
	ds_read_b128 v[52:55], v9 offset:1552
	s_waitcnt lgkmcnt(0)
	v_fmac_f32_e32 v40, v34, v48
	v_fmac_f32_e32 v41, v34, v49
	v_fmac_f32_e32 v42, v34, v50
	v_fmac_f32_e32 v43, v34, v51
	v_fmac_f32_e32 v44, v34, v52
	v_fmac_f32_e32 v45, v34, v53
	v_fmac_f32_e32 v46, v34, v54
	v_fmac_f32_e32 v47, v34, v55
	ds_read_b128 v[48:51], v9 offset:1792
	ds_read_b128 v[52:55], v9 offset:1808
	s_waitcnt lgkmcnt(0)
	v_fmac_f32_e32 v40, v35, v48
	v_fmac_f32_e32 v41, v35, v49
	v_fmac_f32_e32 v42, v35, v50
	v_fmac_f32_e32 v43, v35, v51
	v_fmac_f32_e32 v44, v35, v52
	v_fmac_f32_e32 v45, v35, v53
	v_fmac_f32_e32 v46, v35, v54
	v_fmac_f32_e32 v47, v35, v55
	ds_read_b128 v[48:51], v9 offset:2048
	ds_read_b128 v[52:55], v9 offset:2064
	s_waitcnt lgkmcnt(0)
	v_fmac_f32_e32 v40, v36, v48
	v_fmac_f32_e32 v41, v36, v49
	v_fmac_f32_e32 v42, v36, v50
	v_fmac_f32_e32 v43, v36, v51
	v_fmac_f32_e32 v44, v36, v52
	v_fmac_f32_e32 v45, v36, v53
	v_fmac_f32_e32 v46, v36, v54
	v_fmac_f32_e32 v47, v36, v55
	v_add_u32_e32 v9, 0x900, v9
	s_add_u32 s23, s23, 1
	s_cmp_lt_u32 s23, 3
	s_cbranch_scc1 .Lprep_ci
	v_max_f32_e32 v40, 0, v40
	v_max_f32_e32 v41, 0, v41
	v_max_f32_e32 v42, 0, v42
	v_max_f32_e32 v43, 0, v43
	v_max_f32_e32 v44, 0, v44
	v_max_f32_e32 v45, 0, v45
	v_max_f32_e32 v46, 0, v46
	v_max_f32_e32 v47, 0, v47
	v_cvt_f16_f32_e32 v40, v40
	v_cvt_f16_f32_e32 v41, v41
	v_cvt_f16_f32_e32 v42, v42
	v_cvt_f16_f32_e32 v43, v43
	v_cvt_f16_f32_e32 v44, v44
	v_cvt_f16_f32_e32 v45, v45
	v_cvt_f16_f32_e32 v46, v46
	v_cvt_f16_f32_e32 v47, v47
	v_pack_b32_f16 v40, v40, v41
	v_pack_b32_f16 v41, v42, v43
	v_pack_b32_f16 v42, v44, v45
	v_pack_b32_f16 v43, v46, v47
	v_lshlrev_b32_e32 v5, 7, v5
	v_lshl_add_u32 v5, v4, 4, v5
	s_waitcnt vmcnt(0)
	global_store_dwordx4 v5, v[40:43], s[14:15]
	s_endpgm

	.amdhsa_kernel _Z6prep_k5PrepP
		.amdhsa_group_segment_fixed_size 7168
		.amdhsa_private_segment_fixed_size 0
		.amdhsa_kernarg_size 152
		.amdhsa_user_sgpr_count 2
		.amdhsa_user_sgpr_dispatch_ptr 0
		.amdhsa_user_sgpr_queue_ptr 0
		.amdhsa_user_sgpr_kernarg_segment_ptr 1
		.amdhsa_user_sgpr_dispatch_id 0
		.amdhsa_user_sgpr_kernarg_preload_length 0
		.amdhsa_user_sgpr_kernarg_preload_offset 0
		.amdhsa_user_sgpr_private_segment_size 0
		.amdhsa_uses_dynamic_stack 0
		.amdhsa_enable_private_segment 0
		.amdhsa_system_sgpr_workgroup_id_x 1
		.amdhsa_system_sgpr_workgroup_id_y 0
		.amdhsa_system_sgpr_workgroup_id_z 0
		.amdhsa_system_sgpr_workgroup_info 0
		.amdhsa_system_vgpr_workitem_id 0
		.amdhsa_next_free_vgpr 64
		.amdhsa_next_free_sgpr 64
		.amdhsa_accum_offset 64
		.amdhsa_reserve_vcc 1
		.amdhsa_float_round_mode_32 0
		.amdhsa_float_round_mode_16_64 0
		.amdhsa_float_denorm_mode_32 3
		.amdhsa_float_denorm_mode_16_64 3
		.amdhsa_dx10_clamp 1
		.amdhsa_ieee_mode 1
		.amdhsa_fp16_overflow 0
		.amdhsa_tg_split 0
		.amdhsa_exception_fp_ieee_invalid_op 0
		.amdhsa_exception_fp_denorm_src 0
		.amdhsa_exception_fp_ieee_div_zero 0
		.amdhsa_exception_fp_ieee_overflow 0
		.amdhsa_exception_fp_ieee_underflow 0
		.amdhsa_exception_fp_ieee_inexact 0
		.amdhsa_exception_int_div_zero 0
	.end_amdhsa_kernel

amdhsa.kernels:
  - .agpr_count:     0
    .args:
      - .offset:         0
        .size:           152
        .value_kind:     by_value
    .group_segment_fixed_size: 7168
    .kernarg_segment_align: 8
    .kernarg_segment_size: 152
    .language:       OpenCL C
    .language_version:
      - 2
      - 0
    .max_flat_workgroup_size: 256
    .name:           _Z6prep_k5PrepP
    .private_segment_fixed_size: 0
    .sgpr_count:     70
    .sgpr_spill_count: 0
    .symbol:         _Z6prep_k5PrepP.kd
    .uniform_work_group_size: 1
    .uses_dynamic_stack: false
    .vgpr_count:     64
    .vgpr_spill_count: 0
    .wavefront_size: 64
  - .agpr_count:     0
    .args:
      - .actual_access:  read_only
        .address_space:  global
        .offset:         0
        .size:           8
        .value_kind:     global_buffer
      - .actual_access:  read_only
        .address_space:  global
        .offset:         8
        .size:           8
        .value_kind:     global_buffer
      - .actual_access:  read_only
        .address_space:  global
        .offset:         16
        .size:           8
        .value_kind:     global_buffer
      - .actual_access:  write_only
        .address_space:  global
        .offset:         24
        .size:           8
        .value_kind:     global_buffer
      - .actual_access:  write_only
        .address_space:  global
        .offset:         32
        .size:           8
        .value_kind:     global_buffer
    .group_segment_fixed_size: 9216
    .kernarg_segment_align: 8
    .kernarg_segment_size: 40
    .language:       OpenCL C
    .language_version:
      - 2
      - 0
    .max_flat_workgroup_size: 256
    .name:           _Z8conv1d_kPKDF16_PKfS2_PDF16_S3_
    .private_segment_fixed_size: 0
    .sgpr_count:     22
    .sgpr_spill_count: 0
    .symbol:         _Z8conv1d_kPKDF16_PKfS2_PDF16_S3_.kd
    .uniform_work_group_size: 1
    .uses_dynamic_stack: false
    .vgpr_count:     53
    .vgpr_spill_count: 0
    .wavefront_size: 64
  - .agpr_count:     0
    .args:
      - .actual_access:  read_only
        .address_space:  global
        .offset:         0
        .size:           8
        .value_kind:     global_buffer
      - .actual_access:  read_only
        .address_space:  global
        .offset:         8
        .size:           8
        .value_kind:     global_buffer
      - .actual_access:  read_only
        .address_space:  global
        .offset:         16
        .size:           8
        .value_kind:     global_buffer
      - .actual_access:  read_only
        .address_space:  global
        .offset:         24
        .size:           8
        .value_kind:     global_buffer
      - .actual_access:  write_only
        .address_space:  global
        .offset:         32
        .size:           8
        .value_kind:     global_buffer
      - .actual_access:  write_only
        .address_space:  global
        .offset:         40
        .size:           8
        .value_kind:     global_buffer
    .group_segment_fixed_size: 70656
    .kernarg_segment_align: 8
    .kernarg_segment_size: 48
    .language:       OpenCL C
    .language_version:
      - 2
      - 0
    .max_flat_workgroup_size: 256
    .name:           _Z4dt_kPKfS0_S0_PKDF16_PDF16_S3_
    .private_segment_fixed_size: 0
    .sgpr_count:     25
    .sgpr_spill_count: 0
    .symbol:         _Z4dt_kPKfS0_S0_PKDF16_PDF16_S3_.kd
    .uniform_work_group_size: 1
    .uses_dynamic_stack: false
    .vgpr_count:     96
    .vgpr_spill_count: 0
    .wavefront_size: 64
  - .agpr_count:     0
    .args:
      - .address_space:  global
        .offset:         0
        .size:           8
        .value_kind:     global_buffer
      - .actual_access:  read_only
        .address_space:  global
        .offset:         8
        .size:           8
        .value_kind:     global_buffer
      - .address_space:  global
        .offset:         16
        .size:           8
        .value_kind:     global_buffer
      - .address_space:  global
        .offset:         24
        .size:           8
        .value_kind:     global_buffer
      - .actual_access:  read_only
        .address_space:  global
        .offset:         32
        .size:           8
        .value_kind:     global_buffer
      - .actual_access:  write_only
        .address_space:  global
        .offset:         40
        .size:           8
        .value_kind:     global_buffer
    .group_segment_fixed_size: 86016
    .kernarg_segment_align: 8
    .kernarg_segment_size: 48
    .language:       OpenCL C
    .language_version:
      - 2
      - 0
    .max_flat_workgroup_size: 256
    .name:           _Z6scan_kPKDF16_S0_S0_S0_PKfPf
    .private_segment_fixed_size: 0
    .sgpr_count:     66
    .sgpr_spill_count: 0
    .symbol:         _Z6scan_kPKDF16_S0_S0_S0_PKfPf.kd
    .uniform_work_group_size: 1
    .uses_dynamic_stack: false
    .vgpr_count:     200
    .vgpr_spill_count: 0
    .wavefront_size: 64
  - .agpr_count:     0
    .args:
      - .actual_access:  read_only
        .address_space:  global
        .offset:         0
        .size:           8
        .value_kind:     global_buffer
      - .actual_access:  read_only
        .address_space:  global
        .offset:         8
        .size:           8
        .value_kind:     global_buffer
      - .actual_access:  read_only
        .address_space:  global
        .offset:         16
        .size:           8
        .value_kind:     global_buffer
      - .actual_access:  read_only
        .address_space:  global
        .offset:         24
        .size:           8
        .value_kind:     global_buffer
      - .actual_access:  write_only
        .address_space:  global
        .offset:         32
        .size:           8
        .value_kind:     global_buffer
    .group_segment_fixed_size: 9216
    .kernarg_segment_align: 8
    .kernarg_segment_size: 40
    .language:       OpenCL C
    .language_version:
      - 2
      - 0
    .max_flat_workgroup_size: 256
    .name:           _Z6gate_kPKfPKDF16_S2_S0_PDF16_
    .private_segment_fixed_size: 0
    .sgpr_count:     22
    .sgpr_spill_count: 0
    .symbol:         _Z6gate_kPKfPKDF16_S2_S0_PDF16_.kd
    .uniform_work_group_size: 1
    .uses_dynamic_stack: false
    .vgpr_count:     46
    .vgpr_spill_count: 0
    .wavefront_size: 64
  - .agpr_count:     0
    .args:
      - .actual_access:  read_only
        .address_space:  global
        .offset:         0
        .size:           8
        .value_kind:     global_buffer
      - .actual_access:  read_only
        .address_space:  global
        .offset:         8
        .size:           8
        .value_kind:     global_buffer
      - .actual_access:  read_only
        .address_space:  global
        .offset:         16
        .size:           8
        .value_kind:     global_buffer
      - .actual_access:  write_only
        .address_space:  global
        .offset:         24
        .size:           8
        .value_kind:     global_buffer
    .group_segment_fixed_size: 6912
    .kernarg_segment_align: 8
    .kernarg_segment_size: 32
    .language:       OpenCL C
    .language_version:
      - 2
      - 0
    .max_flat_workgroup_size: 256
    .name:           _Z9deconv3_kPKDF16_PKfS2_Pf
    .private_segment_fixed_size: 0
    .sgpr_count:     26
    .sgpr_spill_count: 0
    .symbol:         _Z9deconv3_kPKDF16_PKfS2_Pf.kd
    .uniform_work_group_size: 1
    .uses_dynamic_stack: false
    .vgpr_count:     55
    .vgpr_spill_count: 0
    .wavefront_size: 64
  - .agpr_count:     8
    .args:
      - .offset:         0
        .size:           112
        .value_kind:     by_value
    .group_segment_fixed_size: 49152
    .kernarg_segment_align: 8
    .kernarg_segment_size: 112
    .language:       OpenCL C
    .language_version:
      - 2
      - 0
    .max_flat_workgroup_size: 256
    .name:           _Z6gemm_gILi32ELi64ELi16ELi32ELi1ELi0ELi64ELi4EEv5GemmP
    .private_segment_fixed_size: 0
    .sgpr_count:     34
    .sgpr_spill_count: 0
    .symbol:         _Z6gemm_gILi32ELi64ELi16ELi32ELi1ELi0ELi64ELi4EEv5GemmP.kd
    .uniform_work_group_size: 1
    .uses_dynamic_stack: false
    .vgpr_count:     40
    .vgpr_spill_count: 0
    .wavefront_size: 64
  - .agpr_count:     16
    .args:
      - .offset:         0
        .size:           112
        .value_kind:     by_value
    .group_segment_fixed_size: 65536
    .kernarg_segment_align: 8
    .kernarg_segment_size: 112
    .language:       OpenCL C
    .language_version:
      - 2
      - 0
    .max_flat_workgroup_size: 256
    .name:           _Z6gemm_gILi64ELi64ELi32ELi32ELi1ELi0ELi64ELi4EEv5GemmP
    .private_segment_fixed_size: 0
    .sgpr_count:     34
    .sgpr_spill_count: 0
    .symbol:         _Z6gemm_gILi64ELi64ELi32ELi32ELi1ELi0ELi64ELi4EEv5GemmP.kd
    .uniform_work_group_size: 1
    .uses_dynamic_stack: false
    .vgpr_count:     56
    .vgpr_spill_count: 0
    .wavefront_size: 64
  - .agpr_count:     32
    .args:
      - .offset:         0
        .size:           112
        .value_kind:     by_value
    .group_segment_fixed_size: 73728
    .kernarg_segment_align: 8
    .kernarg_segment_size: 112
    .language:       OpenCL C
    .language_version:
      - 2
      - 0
    .max_flat_workgroup_size: 256
    .name:           _Z6gemm_gILi64ELi128ELi32ELi64ELi0ELi2ELi64ELi3EEv5GemmP
    .private_segment_fixed_size: 0
    .sgpr_count:     27
    .sgpr_spill_count: 0
    .symbol:         _Z6gemm_gILi64ELi128ELi32ELi64ELi0ELi2ELi64ELi3EEv5GemmP.kd
    .uniform_work_group_size: 1
    .uses_dynamic_stack: false
    .vgpr_count:     80
    .vgpr_spill_count: 0
    .wavefront_size: 64
  - .agpr_count:     16
    .args:
      - .offset:         0
        .size:           112
        .value_kind:     by_value
    .group_segment_fixed_size: 49152
    .kernarg_segment_align: 8
    .kernarg_segment_size: 112
    .language:       OpenCL C
    .language_version:
      - 2
      - 0
    .max_flat_workgroup_size: 256
    .name:           _Z6gemm_gILi64ELi64ELi32ELi32ELi0ELi3ELi64ELi3EEv5GemmP
    .private_segment_fixed_size: 0
    .sgpr_count:     30
    .sgpr_spill_count: 0
    .symbol:         _Z6gemm_gILi64ELi64ELi32ELi32ELi0ELi3ELi64ELi3EEv5GemmP.kd
    .uniform_work_group_size: 1
    .uses_dynamic_stack: false
    .vgpr_count:     56
    .vgpr_spill_count: 0
    .wavefront_size: 64
  - .agpr_count:     16
    .args:
      - .offset:         0
        .size:           112
        .value_kind:     by_value
    .group_segment_fixed_size: 49152
    .kernarg_segment_align: 8
    .kernarg_segment_size: 112
    .language:       OpenCL C
    .language_version:
      - 2
      - 0
    .max_flat_workgroup_size: 256
    .name:           _Z6gemm_gILi64ELi64ELi32ELi32ELi0ELi4ELi64ELi3EEv5GemmP
    .private_segment_fixed_size: 0
    .sgpr_count:     27
    .sgpr_spill_count: 0
    .symbol:         _Z6gemm_gILi64ELi64ELi32ELi32ELi0ELi4ELi64ELi3EEv5GemmP.kd
    .uniform_work_group_size: 1
    .uses_dynamic_stack: false
    .vgpr_count:     52
    .vgpr_spill_count: 0
    .wavefront_size: 64
  - .agpr_count:     8
    .args:
      - .offset:         0
        .size:           112
        .value_kind:     by_value
    .group_segment_fixed_size: 73728
    .kernarg_segment_align: 8
    .kernarg_segment_size: 112
    .language:       OpenCL C
    .language_version:
      - 2
      - 0
    .max_flat_workgroup_size: 256
    .name:           _Z6gemm_gILi32ELi64ELi16ELi32ELi1ELi1ELi128ELi3EEv5GemmP
    .private_segment_fixed_size: 0
    .sgpr_count:     38
    .sgpr_spill_count: 0
    .symbol:         _Z6gemm_gILi32ELi64ELi16ELi32ELi1ELi1ELi128ELi3EEv5GemmP.kd
    .uniform_work_group_size: 1
    .uses_dynamic_stack: false
    .vgpr_count:     48
    .vgpr_spill_count: 0
    .wavefront_size: 64
  - .agpr_count:     0
    .args:
      - .offset:         0
        .size:           112
        .value_kind:     by_value
    .group_segment_fixed_size: 98304
    .kernarg_segment_align: 8
    .kernarg_segment_size: 112
    .language:       OpenCL C
    .language_version:
      - 2
      - 0
    .max_flat_workgroup_size: 256
    .name:           _Z6gemm_gILi32ELi64ELi16ELi32ELi1ELi1ELi64ELi4EEv5GemmP
    .private_segment_fixed_size: 0
    .sgpr_count:     36
    .sgpr_spill_count: 0
    .symbol:         _Z6gemm_gILi32ELi64ELi16ELi32ELi1ELi1ELi64ELi4EEv5GemmP.kd
    .uniform_work_group_size: 1
    .uses_dynamic_stack: false
    .vgpr_count:     148
    .vgpr_spill_count: 0
    .wavefront_size: 64
